# grid barrier: middle arriver of each XCD starts an extra L2 write-back; on top of arrival-counter polling
# baseline (speedup 1.0000x reference)
.LBB0_239:
	s_or_b64 exec, exec, s[2:3]
	v_cvt_f32_u32_e32 v6, v4
	s_waitcnt vmcnt(0)
	v_readfirstlane_b32 s2, v5
	v_sub_u32_e32 v5, 0, v4
	v_rcp_iflag_f32_e32 v6, v6
	v_add_u32_e32 v7, s2, v3
	v_mul_f32_e32 v6, 0x4f7ffffe, v6
	v_cvt_u32_f32_e32 v6, v6
	v_mul_lo_u32 v3, v5, v6
	v_mul_hi_u32 v3, v6, v3
	v_add_u32_e32 v3, v6, v3
	v_mul_hi_u32 v3, v7, v3
	v_mul_lo_u32 v5, v3, v4
	v_sub_u32_e32 v5, v7, v5
	v_add_u32_e32 v6, 1, v3
	v_cmp_ge_u32_e32 vcc, v5, v4
	s_nop 1
	v_cndmask_b32_e32 v3, v3, v6, vcc
	v_sub_u32_e32 v6, v5, v4
	v_cndmask_b32_e32 v5, v5, v6, vcc
	v_add_u32_e32 v6, 1, v3
	v_cmp_ge_u32_e32 vcc, v5, v4
	v_add_u32_e32 v5, 1, v7
	s_nop 0
	v_cndmask_b32_e32 v3, v3, v6, vcc
	v_mul_lo_u32 v6, v4, v3
	v_add_u32_e32 v4, v6, v4
	v_cmp_ne_u32_e32 vcc, v5, v4
	s_and_saveexec_b64 s[2:3], vcc
	s_xor_b64 s[2:3], exec, s[2:3]
	s_cbranch_execz .LBB0_253
	v_readlane_b32 s6, v255, 9
	s_waitcnt lgkmcnt(0)
	v_sub_u32_e32 v2, v4, v6
	v_lshrrev_b32_e32 v2, 1, v2
	v_add_u32_e32 v2, v6, v2
	v_cmp_eq_u32_e32 vcc, v5, v2
	s_cbranch_vccz .Lmidwb_1
	buffer_wbl2 sc1
.Lmidwb_1:
	v_mov_b32_e32 v2, 0x20164
	ds_read_b32 v2, v2
	s_waitcnt lgkmcnt(0)
	v_add_u32_e32 v3, 1, v3
	v_mul_lo_u32 v3, v3, v2
	v_mov_b32_e32 v2, 0x3000
	v_readlane_b32 s7, v255, 10
	s_add_u32 s8, s6, 0x3400
	s_addc_u32 s9, s7, 0
	s_nop 2
	global_load_dword v2, v2, s[6:7] offset:1024 sc1
	s_waitcnt vmcnt(0)
	v_cmp_lt_u32_e32 vcc, v2, v3
	s_and_saveexec_b64 s[6:7], vcc
	s_cbranch_execz .LBB0_252
	s_mov_b32 s10, 1
	s_mov_b64 s[14:15], 0
	v_mov_b32_e32 v2, 0
	s_branch .LBB0_243

.Lmidwb_2:
	v_mov_b32_e32 v2, 0x20164
	ds_read_b32 v2, v2
	s_waitcnt lgkmcnt(0)
	v_add_u32_e32 v3, 1, v3
	v_mul_lo_u32 v3, v3, v2
	v_mov_b32_e32 v2, 0x3000
	v_readlane_b32 s7, v255, 10
	s_add_u32 s8, s6, 0x3400
	s_addc_u32 s9, s7, 0
	s_nop 2
	global_load_dword v2, v2, s[6:7] offset:1024 sc1
	s_waitcnt vmcnt(0)
	v_cmp_lt_u32_e32 vcc, v2, v3
	s_and_saveexec_b64 s[6:7], vcc
	s_cbranch_execz .LBB0_396
	s_mov_b32 s10, 1
	s_mov_b64 s[18:19], 0
	v_mov_b32_e32 v2, 0
	s_branch .LBB0_387

.LBB0_838:
	s_or_b64 exec, exec, s[6:7]
	v_cvt_f32_u32_e32 v6, v4
	s_waitcnt vmcnt(0)
	v_readfirstlane_b32 s6, v5
	v_sub_u32_e32 v5, 0, v4
	v_rcp_iflag_f32_e32 v6, v6
	v_add_u32_e32 v7, s6, v3
	v_mul_f32_e32 v6, 0x4f7ffffe, v6
	v_cvt_u32_f32_e32 v6, v6
	v_mul_lo_u32 v3, v5, v6
	v_mul_hi_u32 v3, v6, v3
	v_add_u32_e32 v3, v6, v3
	v_mul_hi_u32 v3, v7, v3
	v_mul_lo_u32 v5, v3, v4
	v_sub_u32_e32 v5, v7, v5
	v_add_u32_e32 v6, 1, v3
	v_cmp_ge_u32_e32 vcc, v5, v4
	s_nop 1
	v_cndmask_b32_e32 v3, v3, v6, vcc
	v_sub_u32_e32 v6, v5, v4
	v_cndmask_b32_e32 v5, v5, v6, vcc
	v_add_u32_e32 v6, 1, v3
	v_cmp_ge_u32_e32 vcc, v5, v4
	v_add_u32_e32 v5, 1, v7
	s_nop 0
	v_cndmask_b32_e32 v3, v3, v6, vcc
	v_mul_lo_u32 v6, v4, v3
	v_add_u32_e32 v4, v6, v4
	v_cmp_ne_u32_e32 vcc, v5, v4
	s_and_saveexec_b64 s[6:7], vcc
	s_xor_b64 s[6:7], exec, s[6:7]
	s_cbranch_execz .LBB0_852
	v_readlane_b32 s8, v255, 9
	s_waitcnt lgkmcnt(0)
	v_sub_u32_e32 v2, v4, v6
	v_lshrrev_b32_e32 v2, 1, v2
	v_add_u32_e32 v2, v6, v2
	v_cmp_eq_u32_e32 vcc, v5, v2
	s_cbranch_vccz .Lmidwb_3
	buffer_wbl2 sc1
.Lmidwb_3:
	v_mov_b32_e32 v2, 0x20164
	ds_read_b32 v2, v2
	s_waitcnt lgkmcnt(0)
	v_add_u32_e32 v3, 1, v3
	v_mul_lo_u32 v3, v3, v2
	v_mov_b32_e32 v2, 0x3000
	v_readlane_b32 s9, v255, 10
	s_add_u32 s18, s8, 0x3400
	s_addc_u32 s19, s9, 0
	s_nop 2
	global_load_dword v2, v2, s[8:9] offset:1024 sc1
	s_waitcnt vmcnt(0)
	v_cmp_lt_u32_e32 vcc, v2, v3
	s_and_saveexec_b64 s[16:17], vcc
	s_cbranch_execz .LBB0_851
	s_mov_b32 s8, 1
	s_mov_b64 s[20:21], 0
	v_mov_b32_e32 v2, 0
	s_branch .LBB0_842

.Lmidwb_4:
	v_mov_b32_e32 v2, 0x20164
	ds_read_b32 v2, v2
	s_waitcnt lgkmcnt(0)
	v_add_u32_e32 v3, 1, v3
	v_mul_lo_u32 v3, v3, v2
	v_mov_b32_e32 v2, 0x3000
	v_readlane_b32 s9, v255, 10
	s_add_u32 s14, s8, 0x3400
	s_addc_u32 s15, s9, 0
	s_nop 2
	global_load_dword v2, v2, s[8:9] offset:1024 sc1
	s_waitcnt vmcnt(0)
	v_cmp_lt_u32_e32 vcc, v2, v3
	s_and_saveexec_b64 s[8:9], vcc
	s_cbranch_execz .LBB0_931
	s_mov_b32 s10, 1
	s_mov_b64 s[16:17], 0
	v_mov_b32_e32 v2, 0
	s_branch .LBB0_922

.LBB0_998:
	s_or_b64 exec, exec, s[6:7]
	v_cvt_f32_u32_e32 v70, v68
	s_waitcnt vmcnt(0)
	v_readfirstlane_b32 s6, v69
	v_sub_u32_e32 v69, 0, v68
	v_rcp_iflag_f32_e32 v70, v70
	v_add_u32_e32 v71, s6, v67
	v_mul_f32_e32 v70, 0x4f7ffffe, v70
	v_cvt_u32_f32_e32 v70, v70
	v_mul_lo_u32 v67, v69, v70
	v_mul_hi_u32 v67, v70, v67
	v_add_u32_e32 v67, v70, v67
	v_mul_hi_u32 v67, v71, v67
	v_mul_lo_u32 v69, v67, v68
	v_sub_u32_e32 v69, v71, v69
	v_add_u32_e32 v70, 1, v67
	v_cmp_ge_u32_e32 vcc, v69, v68
	s_nop 1
	v_cndmask_b32_e32 v67, v67, v70, vcc
	v_sub_u32_e32 v70, v69, v68
	v_cndmask_b32_e32 v69, v69, v70, vcc
	v_add_u32_e32 v70, 1, v67
	v_cmp_ge_u32_e32 vcc, v69, v68
	v_add_u32_e32 v69, 1, v71
	s_nop 0
	v_cndmask_b32_e32 v67, v67, v70, vcc
	v_mul_lo_u32 v70, v68, v67
	v_add_u32_e32 v68, v70, v68
	v_cmp_ne_u32_e32 vcc, v69, v68
	s_and_saveexec_b64 s[6:7], vcc
	s_xor_b64 s[6:7], exec, s[6:7]
	s_cbranch_execz .LBB0_1012
	v_readlane_b32 s8, v255, 9
	s_waitcnt lgkmcnt(0)
	v_sub_u32_e32 v66, v68, v70
	v_lshrrev_b32_e32 v66, 1, v66
	v_add_u32_e32 v66, v70, v66
	v_cmp_eq_u32_e32 vcc, v69, v66
	s_cbranch_vccz .Lmidwb_5
	buffer_wbl2 sc1
.Lmidwb_5:
	v_mov_b32_e32 v66, 0x20164
	ds_read_b32 v66, v66
	s_waitcnt lgkmcnt(0)
	v_add_u32_e32 v67, 1, v67
	v_mul_lo_u32 v67, v67, v66
	v_mov_b32_e32 v66, 0x3000
	v_readlane_b32 s9, v255, 10
	s_add_u32 s10, s8, 0x3400
	s_addc_u32 s11, s9, 0
	s_nop 2
	global_load_dword v66, v66, s[8:9] offset:1024 sc1
	s_waitcnt vmcnt(0)
	v_cmp_lt_u32_e32 vcc, v66, v67
	s_and_saveexec_b64 s[8:9], vcc
	s_cbranch_execz .LBB0_1011
	s_mov_b32 s22, 1
	s_mov_b64 s[12:13], 0
	v_mov_b32_e32 v66, 0
	s_branch .LBB0_1002

.LBB0_1138:
	s_or_b64 exec, exec, s[4:5]
	v_cvt_f32_u32_e32 v6, v4
	s_waitcnt vmcnt(0)
	v_readfirstlane_b32 s4, v5
	v_sub_u32_e32 v5, 0, v4
	v_rcp_iflag_f32_e32 v6, v6
	v_add_u32_e32 v7, s4, v3
	v_mul_f32_e32 v6, 0x4f7ffffe, v6
	v_cvt_u32_f32_e32 v6, v6
	v_mul_lo_u32 v3, v5, v6
	v_mul_hi_u32 v3, v6, v3
	v_add_u32_e32 v3, v6, v3
	v_mul_hi_u32 v3, v7, v3
	v_mul_lo_u32 v5, v3, v4
	v_sub_u32_e32 v5, v7, v5
	v_add_u32_e32 v6, 1, v3
	v_cmp_ge_u32_e32 vcc, v5, v4
	s_nop 1
	v_cndmask_b32_e32 v3, v3, v6, vcc
	v_sub_u32_e32 v6, v5, v4
	v_cndmask_b32_e32 v5, v5, v6, vcc
	v_add_u32_e32 v6, 1, v3
	v_cmp_ge_u32_e32 vcc, v5, v4
	v_add_u32_e32 v5, 1, v7
	s_nop 0
	v_cndmask_b32_e32 v3, v3, v6, vcc
	v_mul_lo_u32 v6, v4, v3
	v_add_u32_e32 v4, v6, v4
	v_cmp_ne_u32_e32 vcc, v5, v4
	s_and_saveexec_b64 s[4:5], vcc
	s_xor_b64 s[4:5], exec, s[4:5]
	s_cbranch_execz .LBB0_1152
	v_readlane_b32 s6, v255, 9
	s_waitcnt lgkmcnt(0)
	v_sub_u32_e32 v2, v4, v6
	v_lshrrev_b32_e32 v2, 1, v2
	v_add_u32_e32 v2, v6, v2
	v_cmp_eq_u32_e32 vcc, v5, v2
	s_cbranch_vccz .Lmidwb_6
	buffer_wbl2 sc1
.Lmidwb_6:
	v_mov_b32_e32 v2, 0x20164
	ds_read_b32 v2, v2
	s_waitcnt lgkmcnt(0)
	v_add_u32_e32 v3, 1, v3
	v_mul_lo_u32 v3, v3, v2
	v_mov_b32_e32 v2, 0x3000
	v_readlane_b32 s7, v255, 10
	s_add_u32 s8, s6, 0x3400
	s_addc_u32 s9, s7, 0
	s_nop 2
	global_load_dword v2, v2, s[6:7] offset:1024 sc1
	s_waitcnt vmcnt(0)
	v_cmp_lt_u32_e32 vcc, v2, v3
	s_and_saveexec_b64 s[6:7], vcc
	s_cbranch_execz .LBB0_1151
	s_mov_b32 s20, 1
	s_mov_b64 s[10:11], 0
	v_mov_b32_e32 v2, 0
	s_branch .LBB0_1142

.Lmidwb_7:
	v_mov_b32_e32 v2, 0x20164
	ds_read_b32 v2, v2
	s_waitcnt lgkmcnt(0)
	v_add_u32_e32 v3, 1, v3
	v_mul_lo_u32 v3, v3, v2
	v_mov_b32_e32 v2, 0x3000
	v_readlane_b32 s7, v255, 10
	s_add_u32 s12, s6, 0x3400
	s_addc_u32 s13, s7, 0
	s_nop 2
	global_load_dword v2, v2, s[6:7] offset:1024 sc1
	s_waitcnt vmcnt(0)
	v_cmp_lt_u32_e32 vcc, v2, v3
	s_and_saveexec_b64 s[6:7], vcc
	s_cbranch_execz .LBB0_1264
	s_mov_b32 s8, 1
	s_mov_b64 s[14:15], 0
	v_mov_b32_e32 v2, 0
	s_branch .LBB0_1255

.LBB0_1360:
	s_or_b64 exec, exec, s[4:5]
	v_cvt_f32_u32_e32 v4, v2
	s_waitcnt vmcnt(0)
	v_readfirstlane_b32 s4, v3
	v_sub_u32_e32 v3, 0, v2
	v_rcp_iflag_f32_e32 v4, v4
	v_add_u32_e32 v5, s4, v1
	v_mul_f32_e32 v4, 0x4f7ffffe, v4
	v_cvt_u32_f32_e32 v4, v4
	v_mul_lo_u32 v1, v3, v4
	v_mul_hi_u32 v1, v4, v1
	v_add_u32_e32 v1, v4, v1
	v_mul_hi_u32 v1, v5, v1
	v_mul_lo_u32 v3, v1, v2
	v_sub_u32_e32 v3, v5, v3
	v_add_u32_e32 v4, 1, v1
	v_cmp_ge_u32_e32 vcc, v3, v2
	s_nop 1
	v_cndmask_b32_e32 v1, v1, v4, vcc
	v_sub_u32_e32 v4, v3, v2
	v_cndmask_b32_e32 v3, v3, v4, vcc
	v_add_u32_e32 v4, 1, v1
	v_cmp_ge_u32_e32 vcc, v3, v2
	v_add_u32_e32 v3, 1, v5
	s_nop 0
	v_cndmask_b32_e32 v1, v1, v4, vcc
	v_mul_lo_u32 v4, v2, v1
	v_add_u32_e32 v2, v4, v2
	v_cmp_ne_u32_e32 vcc, v3, v2
	s_and_saveexec_b64 s[4:5], vcc
	s_xor_b64 s[4:5], exec, s[4:5]
	s_cbranch_execz .LBB0_1374
	v_readlane_b32 s6, v255, 9
	s_waitcnt lgkmcnt(0)
	v_sub_u32_e32 v0, v2, v4
	v_lshrrev_b32_e32 v0, 1, v0
	v_add_u32_e32 v0, v4, v0
	v_cmp_eq_u32_e32 vcc, v3, v0
	s_cbranch_vccz .Lmidwb_8
	buffer_wbl2 sc1
.Lmidwb_8:
	v_mov_b32_e32 v0, 0x20164
	ds_read_b32 v0, v0
	s_waitcnt lgkmcnt(0)
	v_add_u32_e32 v1, 1, v1
	v_mul_lo_u32 v1, v1, v0
	v_mov_b32_e32 v0, 0x3000
	v_readlane_b32 s7, v255, 10
	s_add_u32 s8, s6, 0x3400
	s_addc_u32 s9, s7, 0
	s_nop 2
	global_load_dword v0, v0, s[6:7] offset:1024 sc1
	s_waitcnt vmcnt(0)
	v_cmp_lt_u32_e32 vcc, v0, v1
	s_and_saveexec_b64 s[6:7], vcc
	s_cbranch_execz .LBB0_1373
	s_mov_b32 s22, 1
	s_mov_b64 s[10:11], 0
	v_mov_b32_e32 v0, 0
	s_branch .LBB0_1364
